# baseline (speedup 1.0000x reference)
_Z13select_kernelPK15HIP_vector_typeIjLj2EEPKfPf:
	s_load_dwordx2 s[38:39], s[0:1], 0x0
	s_load_dwordx2 s[36:37], s[0:1], 0x10
	s_lshr_b32 s3, s2, 3
	s_lshl_b32 s4, s2, 2
	s_and_b32 s4, s4, 28
	s_add_i32 s5, s3, -4
	s_mul_i32 s6, s5, 13
	s_lshr_b32 s6, s6, 6
	s_mul_i32 s7, s6, 5
	s_sub_i32 s7, s5, s7
	s_add_i32 s7, s7, 1
	s_cmp_lt_u32 s3, 4
	s_cselect_b32 s46, 0, s7
	s_cselect_b32 s6, s3, s6
	s_add_i32 s33, s4, s6
	s_cmp_lg_u32 s46, 0
	s_cbranch_scc1 .Lk2_dt
